# baseline (speedup 1.0000x reference)
.LBB7_5:
	s_lshr_b32 s36, s3, 6
	s_lshr_b32 s3, s2, 3
	s_add_i32 s3, s6, s3
	v_and_b32_e32 v8, 63, v0
	s_lshl_b32 s3, s3, 5
	s_lshl_b32 s33, s36, 3
	v_mov_b32_e32 v7, 0
	s_add_i32 s60, s3, s33
	v_min_u32_e32 v1, 8, v8
	v_add_u32_e32 v2, s60, v1
	v_mov_b32_e32 v3, v7
	s_waitcnt lgkmcnt(0)
	v_lshl_add_u64 v[2:3], v[2:3], 2, s[20:21]
	global_load_dword v78, v[2:3], off
	v_and_b32_e32 v79, 15, v0
	s_mov_b32 s31, 0x20000
	s_mov_b32 s38, 0x67c280
	s_and_b32 s37, s23, 0xffff
	v_or_b32_e32 v80, 16, v79
	s_mov_b32 s4, s22
	s_mov_b32 s5, s37
	s_mov_b32 s6, s38
	s_mov_b32 s7, s31
	v_lshrrev_b32_e32 v4, 1, v0
	s_mov_b32 s42, 0xc3500
	s_and_b32 s41, s25, 0xffff
	s_mov_b32 s46, 0x186a00
	s_and_b32 s27, s27, 0xffff
	s_mov_b32 s10, s42
	s_mov_b32 s11, s31
	s_mov_b32 s48, s26
	s_mov_b32 s49, s27
	s_mov_b32 s50, s46
	s_mov_b32 s51, s31
	s_lshl_b32 s21, s60, 4
	v_bfe_u32 v85, v0, 4, 2
	v_lshlrev_b32_e32 v11, 2, v85
	v_lshlrev_b32_e32 v10, 4, v79
	s_and_b32 s29, s29, 0xffff
	s_mov_b32 s43, s31
	s_mov_b32 s40, s24
	s_mov_b32 s47, s31
	v_mov_b32_e32 v93, 0xff800000
	s_waitcnt vmcnt(0)
	v_readlane_b32 s8, v78, 0
	v_readlane_b32 s20, v78, 1
	s_not_b32 s9, s8
	s_add_i32 s9, s20, s9
	v_min_i32_e32 v1, s9, v79
	v_min_i32_e32 v2, s9, v80
	v_add_lshl_u32 v1, v1, s8, 2
	v_add_lshl_u32 v2, v2, s8, 2
	buffer_load_dword v19, v1, s[4:7], 0 offen
	buffer_load_dword v18, v2, s[4:7], 0 offen
	v_lshlrev_b32_e32 v2, 5, v0
	v_and_b32_e32 v6, 0xe0, v2
	v_readlane_b32 s30, v78, 2
	s_not_b32 s39, s20
	v_lshl_add_u64 v[2:3], s[44:45], 0, v[6:7]
	v_and_b32_e32 v6, 16, v4
	s_add_i32 s30, s30, s39
	v_lshrrev_b32_e32 v1, 3, v0
	v_lshl_add_u64 v[2:3], v[2:3], 0, v[6:7]
	v_min_i32_e32 v7, s30, v79
	v_and_b32_e32 v81, 6, v1
	v_min_i32_e32 v9, s30, v80
	v_add_lshl_u32 v7, v7, s20, 2
	s_mov_b32 s8, s24
	s_mov_b32 s9, s41
	global_load_dwordx4 v[2:5], v[2:3], off
	v_add_lshl_u32 v9, v9, s20, 2
	buffer_load_dword v83, v7, s[4:7], 0 offen
	buffer_load_dword v84, v9, s[4:7], 0 offen
	v_lshlrev_b32_e32 v82, 1, v81
	s_mov_b32 s30, 0x30d4000
	s_mov_b32 s39, s31
	s_mov_b32 s44, s26
	s_mov_b32 s45, s27
	s_mov_b32 s20, 0x3e800000
	s_waitcnt vmcnt(4)
	v_lshl_or_b32 v7, v19, 3, v81
	s_waitcnt vmcnt(3)
	v_lshl_or_b32 v9, v18, 3, v81
	buffer_load_ushort v22, v7, s[8:11], 0 offen
	buffer_load_ushort v21, v9, s[8:11], 0 offen
	buffer_load_dword v20, v82, s[48:51], s21 offen
	s_load_dwordx2 s[10:11], s[0:1], 0x68
	s_lshl_b32 s0, s36, 9
	s_add_i32 s4, s0, 0x4200
	s_lshl_b32 s0, s36, 7
	s_add_i32 s5, s0, 0x4a00
	v_cmp_gt_u32_e64 s[0:1], 16, v8
	v_lshlrev_b32_e32 v8, 4, v80
	v_bfe_u32 v9, v0, 3, 2
	v_or3_b32 v88, s4, v8, v11
	v_bfe_u32 v8, v0, 5, 1
	v_and_b32_e32 v7, 31, v0
	v_or3_b32 v86, s4, v10, v11
	v_lshlrev_b32_e32 v10, 2, v9
	v_lshl_or_b32 v90, v8, 2, s5
	v_lshlrev_b32_e32 v8, 4, v8
	s_mov_b32 s36, s22
	s_mov_b32 s21, 0
	v_lshl_or_b32 v87, v79, 2, s5
	v_lshlrev_b32_e32 v89, 4, v7
	v_or3_b32 v91, s4, v8, v10
	v_cmp_gt_u32_e64 s[8:9], 8, v7
	v_cmp_eq_u32_e64 s[4:5], 1, v9
	v_cmp_eq_u32_e64 s[6:7], 2, v9
	v_lshl_or_b32 v92, v7, 5, v6
	s_branch .LBB7_7
.LBB7_6:
	s_or_b64 exec, exec, s[26:27]
	s_cmp_eq_u32 s61, 8
	s_waitcnt vmcnt(0)
	v_mov_b32_e32 v20, v17
	v_mov_b32_e32 v21, v16
	v_mov_b32_e32 v22, v15
	v_mov_b32_e32 v19, v83
	v_mov_b32_e32 v18, v84
	v_mov_b32_e32 v83, v94
	v_mov_b32_e32 v84, v95
	s_mov_b32 s21, s61
	s_cbranch_scc1 .LBB7_91
.LBB7_7:
	s_min_u32 s26, s21, 5
	s_add_i32 s27, s26, 2
	v_readlane_b32 s27, v78, s27
	s_add_i32 s26, s26, 3
	v_readlane_b32 s26, v78, s26
	s_not_b32 s48, s27
	s_add_i32 s26, s26, s48
	s_add_i32 s61, s21, 1
	v_min_i32_e32 v6, s26, v79
	v_min_i32_e32 v7, s26, v80
	s_min_u32 s26, s61, 7
	v_add_lshl_u32 v6, v6, s27, 2
	s_or_b32 s26, s26, s60
	v_add_lshl_u32 v7, v7, s27, 2
	buffer_load_dword v94, v6, s[36:39], 0 offen
	buffer_load_dword v95, v7, s[36:39], 0 offen
	s_waitcnt vmcnt(6)
	v_lshl_or_b32 v6, v83, 3, v81
	s_lshl_b32 s26, s26, 4
	s_waitcnt vmcnt(5)
	v_lshl_or_b32 v7, v84, 3, v81
	buffer_load_ushort v15, v6, s[40:43], 0 offen
	buffer_load_ushort v16, v7, s[40:43], 0 offen
	buffer_load_dword v17, v82, s[44:47], s26 offen
	v_readlane_b32 s63, v78, s21
	v_readlane_b32 s26, v78, s61
	s_sub_i32 s62, s26, s63
	s_cmp_gt_i32 s62, 32
	s_mov_b64 s[26:27], -1
	s_cbranch_scc0 .LBB7_52
	s_add_i32 s64, s62, -1
	s_mov_b32 s26, 0
	v_mov_b32_e32 v6, 0xff800000
.LBB7_9:
	v_add_u32_e32 v7, s26, v79
	v_min_u32_e32 v8, s64, v7
	v_add_u32_e32 v12, 16, v7
	v_add_u32_e32 v8, s63, v8
	v_min_u32_e32 v10, s64, v12
	v_ashrrev_i32_e32 v9, 31, v8
	v_add_u32_e32 v10, s63, v10
	v_lshl_add_u64 v[8:9], v[8:9], 2, s[22:23]
	v_ashrrev_i32_e32 v11, 31, v10
	global_load_dword v13, v[8:9], off
	v_lshl_add_u64 v[8:9], v[10:11], 2, s[22:23]
	global_load_dword v10, v[8:9], off
	v_cmp_gt_u32_e32 vcc, s62, v7
	s_add_i32 s26, s26, 32
	s_cmp_lt_u32 s26, s62
	s_waitcnt vmcnt(1)
	v_lshl_or_b32 v8, v13, 2, v85
	v_ashrrev_i32_e32 v9, 31, v8
	s_waitcnt vmcnt(0)
	v_lshl_or_b32 v10, v10, 2, v85
	v_lshl_add_u64 v[8:9], v[8:9], 1, s[24:25]
	v_ashrrev_i32_e32 v11, 31, v10
	global_load_ushort v13, v[8:9], off
	v_lshl_add_u64 v[8:9], v[10:11], 1, s[24:25]
	global_load_ushort v8, v[8:9], off
	s_waitcnt vmcnt(1)
	v_cvt_f32_f16_e32 v9, v13
	s_waitcnt vmcnt(0)
	v_cvt_f32_f16_e32 v8, v8
	v_add_f32_e32 v9, v20, v9
	v_mul_f32_e32 v10, 0x3e4ccccd, v9
	v_add_f32_e32 v8, v20, v8
	v_max3_f32 v9, v6, v9, v10
	v_mul_f32_e32 v10, 0x3e4ccccd, v8
	v_cndmask_b32_e32 v6, v6, v9, vcc
	v_max3_f32 v7, v6, v8, v10
	v_cmp_gt_u32_e32 vcc, s62, v12
	s_nop 1
	v_cndmask_b32_e32 v6, v6, v7, vcc
	s_cbranch_scc1 .LBB7_9
	s_nop 1
	v_max_f32_dpp v6, v6, v6 quad_perm:[1,0,3,2] row_mask:0xf bank_mask:0xf
	v_mov_b32_e32 v23, 0
	s_nop 1
	v_max_f32_dpp v6, v6, v6 quad_perm:[2,3,0,1] row_mask:0xf bank_mask:0xf
	s_mov_b32 s65, 0
	s_mov_b32 s66, s62
	v_mov_b32_e32 v70, 0
	v_mov_b32_e32 v71, v23
	v_mov_b32_e32 v72, v23
	v_mov_b32_e32 v73, v23
	v_mov_b32_e32 v74, v23
	v_mov_b32_e32 v75, v23
	v_mov_b32_e32 v76, v23
	v_mov_b32_e32 v77, v23
	s_nop 1
	v_max_f32_dpp v6, v6, v6 row_half_mirror row_mask:0xf bank_mask:0xf
	s_nop 0
	s_nop 1
	v_max_f32_dpp v24, v6, v6 row_mirror row_mask:0xf bank_mask:0xf
	s_branch .LBB7_12
.LBB7_11:
	s_waitcnt vmcnt(0)
	v_add_f32_e32 v6, v25, v26
	s_add_i32 s65, s65, 32
	s_sub_i32 s66, s66, 32
	s_cmp_lt_u32 s65, s62
	v_add_f32_e32 v23, v23, v6
	s_cbranch_scc0 .LBB7_51
.LBB7_12:
	v_add_u32_e32 v8, s65, v79
	v_add_u32_e32 v9, 16, v8
	v_min_i32_e32 v6, s64, v8
	v_add_u32_e32 v6, s63, v6
	v_min_i32_e32 v10, s64, v9
	v_ashrrev_i32_e32 v7, 31, v6
	v_add_u32_e32 v10, s63, v10
	v_lshl_add_u64 v[6:7], v[6:7], 2, s[22:23]
	v_ashrrev_i32_e32 v11, 31, v10
	v_lshl_add_u64 v[10:11], v[10:11], 2, s[22:23]
	global_load_dword v7, v[6:7], off
	s_nop 0
	global_load_dword v6, v[10:11], off
	v_cmp_gt_u32_e32 vcc, s62, v8
	v_mov_b32_e32 v8, 0xff800000
	v_mov_b32_e32 v10, 0xff800000
	s_and_saveexec_b64 s[26:27], vcc
	s_cbranch_execz .LBB7_14
	s_waitcnt vmcnt(1)
	v_lshl_or_b32 v10, v7, 2, v85
	v_ashrrev_i32_e32 v11, 31, v10
	v_lshl_add_u64 v[10:11], v[10:11], 1, s[24:25]
	global_load_ushort v10, v[10:11], off
	s_waitcnt vmcnt(0)
	v_cvt_f32_f16_e32 v10, v10
	v_add_f32_e32 v10, v20, v10
	v_mul_f32_e32 v11, 0x3e4ccccd, v10
	v_max_f32_e32 v10, v10, v11
.LBB7_14:
	s_or_b64 exec, exec, s[26:27]
	v_cmp_gt_u32_e32 vcc, s62, v9
	s_and_saveexec_b64 s[26:27], vcc
	s_cbranch_execz .LBB7_16
	s_waitcnt vmcnt(0)
	v_lshl_or_b32 v8, v6, 2, v85
	v_ashrrev_i32_e32 v9, 31, v8
	v_lshl_add_u64 v[8:9], v[8:9], 1, s[24:25]
	global_load_ushort v8, v[8:9], off
	s_waitcnt vmcnt(0)
	v_cvt_f32_f16_e32 v8, v8
	v_add_f32_e32 v8, v20, v8
	v_mul_f32_e32 v9, 0x3e4ccccd, v8
	v_max_f32_e32 v8, v8, v9
.LBB7_16:
	s_or_b64 exec, exec, s[26:27]
	v_sub_f32_e32 v9, v10, v24
	v_mul_f32_e32 v9, 0x3fb8aa3b, v9
	v_exp_f32_e32 v25, v9
	ds_write_b32 v86, v25
	s_and_saveexec_b64 s[26:27], s[0:1]
	s_cbranch_execz .LBB7_18
	s_waitcnt vmcnt(1)
	ds_write_b32 v87, v7
.LBB7_18:
	s_or_b64 exec, exec, s[26:27]
	s_waitcnt vmcnt(1)
	v_sub_f32_e32 v7, v8, v24
	v_mul_f32_e32 v7, 0x3fb8aa3b, v7
	v_exp_f32_e32 v26, v7
	s_cmp_lt_i32 s66, 17
	s_cbranch_scc1 .LBB7_22
	ds_write_b32 v88, v26
	s_and_saveexec_b64 s[26:27], s[0:1]
	s_cbranch_execz .LBB7_21
	s_waitcnt vmcnt(0)
	ds_write_b32 v87, v6 offset:64

.LBB7_22:
	s_min_i32 s26, s66, 32
	s_add_i32 s26, s26, 3
	s_ashr_i32 s67, s26, 2
	s_cmp_lt_i32 s67, 1
	s_cbranch_scc1 .LBB7_11
	s_waitcnt vmcnt(0)
	s_min_u32 s27, s67, 4
	s_lshl_b32 s48, s27, 4
	s_add_i32 s48, s48, -64
	v_add_u32_e32 v38, s48, v90
	s_lshl_b32 s48, s48, 2
	v_add_u32_e32 v39, s48, v91
	ds_read2_b32 v[30:31], v39 offset0:0 offset1:8
	ds_read2_b32 v[32:33], v39 offset0:16 offset1:24
	ds_read2_b32 v[34:35], v39 offset0:32 offset1:40
	ds_read2_b32 v[36:37], v39 offset0:48 offset1:56
	ds_read2_b32 v[6:7], v38 offset0:0 offset1:2
	ds_read2_b32 v[8:9], v38 offset0:4 offset1:6
	ds_read2_b32 v[10:11], v38 offset0:8 offset1:10
	ds_read2_b32 v[12:13], v38 offset0:12 offset1:14
	s_waitcnt lgkmcnt(0)
	s_cmp_eq_u32 s27, 1
	s_cbranch_scc1 .Lagg2g_b0_i0
	s_cmp_eq_u32 s27, 2
	s_cbranch_scc1 .Lagg2g_b0_i1
	s_cmp_eq_u32 s27, 3
	s_cbranch_scc1 .Lagg2g_b0_i2
	v_lshl_or_b32 v6, v6, 9, v89
	v_lshl_or_b32 v7, v7, 9, v89
	buffer_load_dwordx4 v[66:69], v6, s[28:31], 0 offen sc0 sc1
	buffer_load_dwordx4 v[62:65], v7, s[28:31], 0 offen sc0 sc1
.Lagg2g_b0_i2:
	v_lshl_or_b32 v8, v8, 9, v89
	v_lshl_or_b32 v9, v9, 9, v89
	buffer_load_dwordx4 v[58:61], v8, s[28:31], 0 offen sc0 sc1
	buffer_load_dwordx4 v[54:57], v9, s[28:31], 0 offen sc0 sc1
.Lagg2g_b0_i1:
	v_lshl_or_b32 v10, v10, 9, v89
	v_lshl_or_b32 v11, v11, 9, v89
	buffer_load_dwordx4 v[50:53], v10, s[28:31], 0 offen sc0 sc1
	buffer_load_dwordx4 v[46:49], v11, s[28:31], 0 offen sc0 sc1
.Lagg2g_b0_i0:
	v_lshl_or_b32 v12, v12, 9, v89
	v_lshl_or_b32 v13, v13, 9, v89
	buffer_load_dwordx4 v[42:45], v12, s[28:31], 0 offen sc0 sc1
	buffer_load_dwordx4 v[38:41], v13, s[28:31], 0 offen sc0 sc1
	s_cmp_eq_u32 s27, 1
	s_cbranch_scc1 .Lagg2g_b0_f0
	s_cmp_eq_u32 s27, 2
	s_cbranch_scc1 .Lagg2g_b0_f1
	s_cmp_eq_u32 s27, 3
	s_cbranch_scc1 .Lagg2g_b0_f2
	s_waitcnt vmcnt(7)
	v_fma_mix_f32 v70, v30, v66, v70 op_sel_hi:[0,1,0]
	v_fma_mix_f32 v71, v30, v66, v71 op_sel:[0,1,0] op_sel_hi:[0,1,0]
	v_fma_mix_f32 v72, v30, v67, v72 op_sel_hi:[0,1,0]
	v_fma_mix_f32 v73, v30, v67, v73 op_sel:[0,1,0] op_sel_hi:[0,1,0]
	v_fma_mix_f32 v74, v30, v68, v74 op_sel_hi:[0,1,0]
	v_fma_mix_f32 v75, v30, v68, v75 op_sel:[0,1,0] op_sel_hi:[0,1,0]
	v_fma_mix_f32 v76, v30, v69, v76 op_sel_hi:[0,1,0]
	v_fma_mix_f32 v77, v30, v69, v77 op_sel:[0,1,0] op_sel_hi:[0,1,0]
	s_waitcnt vmcnt(6)
	v_fma_mix_f32 v70, v31, v62, v70 op_sel_hi:[0,1,0]
	v_fma_mix_f32 v71, v31, v62, v71 op_sel:[0,1,0] op_sel_hi:[0,1,0]
	v_fma_mix_f32 v72, v31, v63, v72 op_sel_hi:[0,1,0]
	v_fma_mix_f32 v73, v31, v63, v73 op_sel:[0,1,0] op_sel_hi:[0,1,0]
	v_fma_mix_f32 v74, v31, v64, v74 op_sel_hi:[0,1,0]
	v_fma_mix_f32 v75, v31, v64, v75 op_sel:[0,1,0] op_sel_hi:[0,1,0]
	v_fma_mix_f32 v76, v31, v65, v76 op_sel_hi:[0,1,0]
	v_fma_mix_f32 v77, v31, v65, v77 op_sel:[0,1,0] op_sel_hi:[0,1,0]

.Lagg2g_b0_f0:
	s_waitcnt vmcnt(1)
	v_fma_mix_f32 v70, v36, v42, v70 op_sel_hi:[0,1,0]
	v_fma_mix_f32 v71, v36, v42, v71 op_sel:[0,1,0] op_sel_hi:[0,1,0]
	v_fma_mix_f32 v72, v36, v43, v72 op_sel_hi:[0,1,0]
	v_fma_mix_f32 v73, v36, v43, v73 op_sel:[0,1,0] op_sel_hi:[0,1,0]
	v_fma_mix_f32 v74, v36, v44, v74 op_sel_hi:[0,1,0]
	v_fma_mix_f32 v75, v36, v44, v75 op_sel:[0,1,0] op_sel_hi:[0,1,0]
	v_fma_mix_f32 v76, v36, v45, v76 op_sel_hi:[0,1,0]
	v_fma_mix_f32 v77, v36, v45, v77 op_sel:[0,1,0] op_sel_hi:[0,1,0]
	s_waitcnt vmcnt(0)
	v_fma_mix_f32 v70, v37, v38, v70 op_sel_hi:[0,1,0]
	v_fma_mix_f32 v71, v37, v38, v71 op_sel:[0,1,0] op_sel_hi:[0,1,0]
	v_fma_mix_f32 v72, v37, v39, v72 op_sel_hi:[0,1,0]
	v_fma_mix_f32 v73, v37, v39, v73 op_sel:[0,1,0] op_sel_hi:[0,1,0]
	v_fma_mix_f32 v74, v37, v40, v74 op_sel_hi:[0,1,0]
	v_fma_mix_f32 v75, v37, v40, v75 op_sel:[0,1,0] op_sel_hi:[0,1,0]
	v_fma_mix_f32 v76, v37, v41, v76 op_sel_hi:[0,1,0]
	v_fma_mix_f32 v77, v37, v41, v77 op_sel:[0,1,0] op_sel_hi:[0,1,0]
	s_cmp_lt_u32 s67, 5
	s_cbranch_scc1 .Lagg2g_done
	s_add_i32 s27, s67, -4
	s_lshl_b32 s48, s27, 4
	s_add_i32 s48, s48, 0
	v_add_u32_e32 v38, s48, v90
	s_lshl_b32 s48, s48, 2
	v_add_u32_e32 v39, s48, v91
	ds_read2_b32 v[30:31], v39 offset0:0 offset1:8
	ds_read2_b32 v[32:33], v39 offset0:16 offset1:24
	ds_read2_b32 v[34:35], v39 offset0:32 offset1:40
	ds_read2_b32 v[36:37], v39 offset0:48 offset1:56
	ds_read2_b32 v[6:7], v38 offset0:0 offset1:2
	ds_read2_b32 v[8:9], v38 offset0:4 offset1:6
	ds_read2_b32 v[10:11], v38 offset0:8 offset1:10
	ds_read2_b32 v[12:13], v38 offset0:12 offset1:14
	s_waitcnt lgkmcnt(0)
	s_cmp_eq_u32 s27, 1
	s_cbranch_scc1 .Lagg2g_b1_i0
	s_cmp_eq_u32 s27, 2
	s_cbranch_scc1 .Lagg2g_b1_i1
	s_cmp_eq_u32 s27, 3
	s_cbranch_scc1 .Lagg2g_b1_i2
	v_lshl_or_b32 v6, v6, 9, v89
	v_lshl_or_b32 v7, v7, 9, v89
	buffer_load_dwordx4 v[66:69], v6, s[28:31], 0 offen sc0 sc1
	buffer_load_dwordx4 v[62:65], v7, s[28:31], 0 offen sc0 sc1

.LBB7_51:
	s_nop 1
	v_add_f32_dpp v6, v23, v23 quad_perm:[1,0,3,2] row_mask:0xf bank_mask:0xf
	s_nop 0
	s_nop 1
	v_add_f32_dpp v6, v6, v6 quad_perm:[2,3,0,1] row_mask:0xf bank_mask:0xf
	s_nop 0
	s_nop 1
	v_add_f32_dpp v6, v6, v6 row_half_mirror row_mask:0xf bank_mask:0xf
	s_nop 0
	s_nop 1
	v_add_f32_dpp v6, v6, v6 row_mirror row_mask:0xf bank_mask:0xf
	s_nop 0
	v_readlane_b32 s48, v6, 32
	v_readlane_b32 s49, v6, 48
	v_readlane_b32 s26, v6, 0
	v_readlane_b32 s27, v6, 16
	v_mov_b32_e32 v6, s49
	v_mov_b32_e32 v7, s48
	v_cndmask_b32_e64 v6, v6, v7, s[6:7]
	v_mov_b32_e32 v7, s27
	v_cndmask_b32_e64 v6, v6, v7, s[4:5]
	v_mov_b32_e32 v7, s26
	v_cndmask_b32_e64 v6, v6, v7, s[8:9]
	v_rcp_f32_e32 v6, v6
	s_mov_b64 s[26:27], 0
	v_pk_mul_f32 v[76:77], v[6:7], v[76:77] op_sel_hi:[0,1]
	v_pk_mul_f32 v[74:75], v[6:7], v[74:75] op_sel_hi:[0,1]
	v_pk_mul_f32 v[72:73], v[6:7], v[72:73] op_sel_hi:[0,1]
	v_pk_mul_f32 v[70:71], v[6:7], v[70:71] op_sel_hi:[0,1]
.LBB7_52:
	s_and_b64 vcc, exec, s[26:27]
	s_cbranch_vccz .LBB7_89
	s_waitcnt vmcnt(7)
	v_cvt_f32_f16_e32 v6, v22
	s_waitcnt vmcnt(6)
	v_cvt_f32_f16_e32 v7, v21
	v_cmp_gt_i32_e32 vcc, s62, v79
	s_waitcnt vmcnt(5)
	v_add_f32_e32 v6, v20, v6
	v_add_f32_e32 v7, v20, v7
	v_mul_f32_e32 v8, 0x3e4ccccd, v6
	v_max_f32_e32 v6, v6, v8
	v_mul_f32_e32 v8, 0x3e4ccccd, v7
	v_cndmask_b32_e32 v6, v93, v6, vcc
	v_max_f32_e32 v7, v7, v8
	v_cmp_gt_i32_e32 vcc, s62, v80
	s_nop 1
	v_cndmask_b32_e32 v7, v93, v7, vcc
	v_max_f32_e32 v8, v6, v7
	s_nop 1
	v_max_f32_dpp v8, v8, v8 quad_perm:[1,0,3,2] row_mask:0xf bank_mask:0xf
	s_nop 0
	s_nop 1
	v_max_f32_dpp v8, v8, v8 quad_perm:[2,3,0,1] row_mask:0xf bank_mask:0xf
	s_nop 0
	s_nop 1
	v_max_f32_dpp v8, v8, v8 row_half_mirror row_mask:0xf bank_mask:0xf
	s_nop 0
	s_nop 1
	v_max_f32_dpp v8, v8, v8 row_mirror row_mask:0xf bank_mask:0xf
	s_nop 0
	v_sub_f32_e32 v6, v6, v8
	v_mul_f32_e32 v6, 0x3fb8aa3b, v6
	v_exp_f32_e32 v9, v6
	v_sub_f32_e32 v6, v7, v8
	v_mul_f32_e32 v6, 0x3fb8aa3b, v6
	v_exp_f32_e32 v6, v6
	s_nop 0
	v_add_f32_e32 v7, v9, v6
	s_nop 1
	v_add_f32_dpp v7, v7, v7 quad_perm:[1,0,3,2] row_mask:0xf bank_mask:0xf
	s_nop 0
	s_nop 1
	v_add_f32_dpp v7, v7, v7 quad_perm:[2,3,0,1] row_mask:0xf bank_mask:0xf
	s_nop 0
	s_nop 1
	v_add_f32_dpp v7, v7, v7 row_half_mirror row_mask:0xf bank_mask:0xf
	s_nop 0
	s_nop 1
	v_add_f32_dpp v7, v7, v7 row_mirror row_mask:0xf bank_mask:0xf
	s_nop 0
	v_rcp_f32_e32 v7, v7
	s_nop 0
	v_mul_f32_e32 v8, v9, v7
	ds_write_b32 v86, v8
	s_and_saveexec_b64 s[26:27], s[0:1]
	ds_write_b32 v87, v19
	s_or_b64 exec, exec, s[26:27]
	s_cmp_lt_i32 s62, 17
	s_cbranch_scc1 .LBB7_59
	v_mul_f32_e32 v6, v6, v7
	ds_write_b32 v88, v6
	s_and_saveexec_b64 s[26:27], s[0:1]
	ds_write_b32 v87, v18 offset:64
	s_or_b64 exec, exec, s[26:27]
.LBB7_59:
	s_add_i32 s62, s62, 3
	s_ashr_i32 s62, s62, 2
	s_cmp_lt_i32 s62, 1
	s_cbranch_scc1 .LBB7_88
	v_mov_b32_e32 v70, 0
	v_mov_b32_e32 v71, 0
	v_mov_b32_e32 v72, 0
	v_mov_b32_e32 v73, 0
	v_mov_b32_e32 v74, 0
	v_mov_b32_e32 v75, 0
	v_mov_b32_e32 v76, 0
	v_mov_b32_e32 v77, 0
	s_min_u32 s27, s62, 4
	s_lshl_b32 s48, s27, 4
	s_add_i32 s48, s48, -64
	v_add_u32_e32 v38, s48, v90
	s_lshl_b32 s48, s48, 2
	v_add_u32_e32 v39, s48, v91
	ds_read2_b32 v[30:31], v39 offset0:0 offset1:8
	ds_read2_b32 v[32:33], v39 offset0:16 offset1:24
	ds_read2_b32 v[34:35], v39 offset0:32 offset1:40
	ds_read2_b32 v[36:37], v39 offset0:48 offset1:56
	ds_read2_b32 v[6:7], v38 offset0:0 offset1:2
	ds_read2_b32 v[8:9], v38 offset0:4 offset1:6
	ds_read2_b32 v[10:11], v38 offset0:8 offset1:10
	ds_read2_b32 v[12:13], v38 offset0:12 offset1:14
	s_waitcnt lgkmcnt(0)
	s_cmp_eq_u32 s27, 1
	s_cbranch_scc1 .Lagg2f_b0_i0
	s_cmp_eq_u32 s27, 2
	s_cbranch_scc1 .Lagg2f_b0_i1
	s_cmp_eq_u32 s27, 3
	s_cbranch_scc1 .Lagg2f_b0_i2
	v_lshl_or_b32 v6, v6, 9, v89
	v_lshl_or_b32 v7, v7, 9, v89
	buffer_load_dwordx4 v[66:69], v6, s[28:31], 0 offen sc0 sc1
	buffer_load_dwordx4 v[62:65], v7, s[28:31], 0 offen sc0 sc1

.Lagg2f_b0_f0:
	s_waitcnt vmcnt(1)
	v_fma_mix_f32 v70, v36, v42, v70 op_sel_hi:[0,1,0]
	v_fma_mix_f32 v71, v36, v42, v71 op_sel:[0,1,0] op_sel_hi:[0,1,0]
	v_fma_mix_f32 v72, v36, v43, v72 op_sel_hi:[0,1,0]
	v_fma_mix_f32 v73, v36, v43, v73 op_sel:[0,1,0] op_sel_hi:[0,1,0]
	v_fma_mix_f32 v74, v36, v44, v74 op_sel_hi:[0,1,0]
	v_fma_mix_f32 v75, v36, v44, v75 op_sel:[0,1,0] op_sel_hi:[0,1,0]
	v_fma_mix_f32 v76, v36, v45, v76 op_sel_hi:[0,1,0]
	v_fma_mix_f32 v77, v36, v45, v77 op_sel:[0,1,0] op_sel_hi:[0,1,0]
	s_waitcnt vmcnt(0)
	v_fma_mix_f32 v70, v37, v38, v70 op_sel_hi:[0,1,0]
	v_fma_mix_f32 v71, v37, v38, v71 op_sel:[0,1,0] op_sel_hi:[0,1,0]
	v_fma_mix_f32 v72, v37, v39, v72 op_sel_hi:[0,1,0]
	v_fma_mix_f32 v73, v37, v39, v73 op_sel:[0,1,0] op_sel_hi:[0,1,0]
	v_fma_mix_f32 v74, v37, v40, v74 op_sel_hi:[0,1,0]
	v_fma_mix_f32 v75, v37, v40, v75 op_sel:[0,1,0] op_sel_hi:[0,1,0]
	v_fma_mix_f32 v76, v37, v41, v76 op_sel_hi:[0,1,0]
	v_fma_mix_f32 v77, v37, v41, v77 op_sel:[0,1,0] op_sel_hi:[0,1,0]
	s_cmp_lt_u32 s62, 5
	s_cbranch_scc1 .Lagg2f_done
	s_add_i32 s27, s62, -4
	s_lshl_b32 s48, s27, 4
	s_add_i32 s48, s48, 0
	v_add_u32_e32 v38, s48, v90
	s_lshl_b32 s48, s48, 2
	v_add_u32_e32 v39, s48, v91
	ds_read2_b32 v[30:31], v39 offset0:0 offset1:8
	ds_read2_b32 v[32:33], v39 offset0:16 offset1:24
	ds_read2_b32 v[34:35], v39 offset0:32 offset1:40
	ds_read2_b32 v[36:37], v39 offset0:48 offset1:56
	ds_read2_b32 v[6:7], v38 offset0:0 offset1:2
	ds_read2_b32 v[8:9], v38 offset0:4 offset1:6
	ds_read2_b32 v[10:11], v38 offset0:8 offset1:10
	ds_read2_b32 v[12:13], v38 offset0:12 offset1:14
	s_waitcnt lgkmcnt(0)
	s_cmp_eq_u32 s27, 1
	s_cbranch_scc1 .Lagg2f_b1_i0
	s_cmp_eq_u32 s27, 2
	s_cbranch_scc1 .Lagg2f_b1_i1
	s_cmp_eq_u32 s27, 3
	s_cbranch_scc1 .Lagg2f_b1_i2
	v_lshl_or_b32 v6, v6, 9, v89
	v_lshl_or_b32 v7, v7, 9, v89
	buffer_load_dwordx4 v[66:69], v6, s[28:31], 0 offen sc0 sc1
	buffer_load_dwordx4 v[62:65], v7, s[28:31], 0 offen sc0 sc1

.LBB7_88:
	v_mov_b32_e32 v77, 0
	v_mov_b32_e32 v76, 0
	v_mov_b32_e32 v75, 0
	v_mov_b32_e32 v74, 0
	v_mov_b32_e32 v73, 0
	v_mov_b32_e32 v72, 0
	v_mov_b32_e32 v71, 0
	v_mov_b32_e32 v70, 0
.LBB7_89:
	s_nop 1
	v_permlane32_swap_b32 v70, v74
	s_nop 1
	v_permlane32_swap_b32 v71, v75
	s_nop 1
	v_permlane32_swap_b32 v72, v76
	s_nop 1
	v_permlane32_swap_b32 v73, v77
	s_nop 0
	v_add_f32_e32 v6, v70, v74
	v_mov_b32_e32 v8, v6
	v_add_f32_e32 v7, v71, v75
	v_add_f32_e32 v10, v72, v76
	v_mov_b32_dpp v8, v8 row_ror:8 row_mask:0xf bank_mask:0xf
	v_add_f32_e32 v8, v6, v8
	v_mov_b32_e32 v6, v7
	v_add_f32_e32 v11, v73, v77
	s_nop 0
	v_mov_b32_dpp v6, v6 row_ror:8 row_mask:0xf bank_mask:0xf
	v_add_f32_e32 v9, v7, v6
	v_mov_b32_e32 v6, v10
	v_mov_b32_e32 v7, v11
	s_nop 0
	v_mov_b32_dpp v6, v6 row_ror:8 row_mask:0xf bank_mask:0xf
	v_mov_b32_dpp v7, v7 row_ror:8 row_mask:0xf bank_mask:0xf
	v_add_f32_e32 v6, v10, v6
	v_add_f32_e32 v7, v11, v7
	v_mov_b32_e32 v10, v8
	v_mov_b32_e32 v11, v9
	v_mov_b32_e32 v12, v6
	v_mov_b32_e32 v13, v7
	s_nop 1
	v_permlane16_swap_b32 v8, v10
	s_nop 1
	v_permlane16_swap_b32 v9, v11
	s_nop 1
	v_permlane16_swap_b32 v6, v12
	s_nop 1
	v_permlane16_swap_b32 v7, v13
	s_and_saveexec_b64 s[26:27], s[8:9]
	s_cbranch_execz .LBB7_6
	s_add_i32 s21, s21, s33
	s_mulk_i32 s21, 0x110
	v_pk_add_f32 v[8:9], v[8:9], v[10:11]
	v_pk_add_f32 v[6:7], v[6:7], v[12:13]
	v_add_u32_e32 v14, s21, v92
	v_pk_fma_f32 v[8:9], v[8:9], s[20:21], v[2:3] op_sel_hi:[1,0,1]
	v_pk_fma_f32 v[10:11], v[6:7], s[20:21], v[4:5] op_sel_hi:[1,0,1]
	ds_write_b128 v14, v[8:11]
	s_branch .LBB7_6

.LBB7_93:
	v_lshl_add_u64 v[70:71], v[6:7], 0, s[4:5]
	global_load_dwordx4 v[10:13], v[70:71], off
	global_load_dwordx4 v[14:17], v[70:71], off offset:128
	global_load_dwordx4 v[18:21], v[70:71], off offset:256
	global_load_dwordx4 v[22:25], v[70:71], off offset:384
	global_load_dwordx4 v[26:29], v[70:71], off offset:512
	global_load_dwordx4 v[30:33], v[70:71], off offset:640
	global_load_dwordx4 v[34:37], v[70:71], off offset:768
	global_load_dwordx4 v[38:41], v[70:71], off offset:896
	global_load_dwordx4 v[42:45], v[70:71], off offset:1024
	global_load_dwordx4 v[46:49], v[70:71], off offset:1152
	global_load_dwordx4 v[50:53], v[70:71], off offset:1280
	global_load_dwordx4 v[54:57], v[70:71], off offset:1408
	global_load_dwordx4 v[58:61], v[70:71], off offset:1536
	global_load_dwordx4 v[62:65], v[70:71], off offset:1664
	global_load_dwordx4 v[66:69], v[70:71], off offset:1792
	s_nop 0
	global_load_dwordx4 v[70:73], v[70:71], off offset:1920
	ds_read_b128 v[74:77], v9
	ds_read_b128 v[78:81], v9 offset:16
	ds_read_b128 v[82:85], v9 offset:32
	ds_read_b128 v[86:89], v9 offset:48
	s_add_u32 s4, s4, 0x800
	s_waitcnt lgkmcnt(3)
	v_mov_b32_e32 v90, v77
	s_waitcnt lgkmcnt(2)
	v_mov_b32_e32 v92, v81
	s_waitcnt lgkmcnt(1)
	v_mov_b32_e32 v94, v85
	s_addc_u32 s5, s5, 0
	s_waitcnt lgkmcnt(0)
	s_nop 0
	v_add_u32_e32 v9, 64, v9
	s_cmpk_eq_i32 s4, 0x2000
	s_waitcnt vmcnt(15)
	v_pk_fma_f32 v[2:3], v[74:75], v[10:11], v[2:3] op_sel_hi:[0,1,1]
	v_pk_fma_f32 v[4:5], v[74:75], v[12:13], v[4:5] op_sel_hi:[0,1,1]
	s_waitcnt vmcnt(14)
	v_pk_fma_f32 v[2:3], v[74:75], v[14:15], v[2:3] op_sel:[1,0,0]
	v_pk_fma_f32 v[4:5], v[74:75], v[16:17], v[4:5] op_sel:[1,0,0]
	s_waitcnt vmcnt(13)
	v_pk_fma_f32 v[2:3], v[76:77], v[18:19], v[2:3] op_sel_hi:[0,1,1]
	v_pk_fma_f32 v[4:5], v[76:77], v[20:21], v[4:5] op_sel_hi:[0,1,1]
	s_waitcnt vmcnt(12)
	v_pk_fma_f32 v[2:3], v[90:91], v[22:23], v[2:3] op_sel_hi:[0,1,1]
	v_pk_fma_f32 v[4:5], v[90:91], v[24:25], v[4:5] op_sel_hi:[0,1,1]
	s_waitcnt vmcnt(11)
	v_pk_fma_f32 v[2:3], v[78:79], v[26:27], v[2:3] op_sel_hi:[0,1,1]
	v_pk_fma_f32 v[4:5], v[78:79], v[28:29], v[4:5] op_sel_hi:[0,1,1]
	s_waitcnt vmcnt(10)
	v_pk_fma_f32 v[2:3], v[78:79], v[30:31], v[2:3] op_sel:[1,0,0]
	v_pk_fma_f32 v[4:5], v[78:79], v[32:33], v[4:5] op_sel:[1,0,0]
	s_waitcnt vmcnt(9)
	v_pk_fma_f32 v[2:3], v[80:81], v[34:35], v[2:3] op_sel_hi:[0,1,1]
	v_pk_fma_f32 v[4:5], v[80:81], v[36:37], v[4:5] op_sel_hi:[0,1,1]
	s_waitcnt vmcnt(8)
	v_pk_fma_f32 v[2:3], v[92:93], v[38:39], v[2:3] op_sel_hi:[0,1,1]
	v_pk_fma_f32 v[4:5], v[92:93], v[40:41], v[4:5] op_sel_hi:[0,1,1]
	s_waitcnt vmcnt(7)
	v_pk_fma_f32 v[2:3], v[82:83], v[42:43], v[2:3] op_sel_hi:[0,1,1]
	v_pk_fma_f32 v[4:5], v[82:83], v[44:45], v[4:5] op_sel_hi:[0,1,1]
	s_waitcnt vmcnt(6)
	v_pk_fma_f32 v[2:3], v[82:83], v[46:47], v[2:3] op_sel:[1,0,0]
	v_pk_fma_f32 v[4:5], v[82:83], v[48:49], v[4:5] op_sel:[1,0,0]
	s_waitcnt vmcnt(5)
	v_pk_fma_f32 v[2:3], v[84:85], v[50:51], v[2:3] op_sel_hi:[0,1,1]
	v_pk_fma_f32 v[4:5], v[84:85], v[52:53], v[4:5] op_sel_hi:[0,1,1]
	s_waitcnt vmcnt(4)
	v_pk_fma_f32 v[2:3], v[94:95], v[54:55], v[2:3] op_sel_hi:[0,1,1]
	v_pk_fma_f32 v[4:5], v[94:95], v[56:57], v[4:5] op_sel_hi:[0,1,1]
	s_waitcnt vmcnt(3)
	v_pk_fma_f32 v[2:3], v[86:87], v[58:59], v[2:3] op_sel_hi:[0,1,1]
	v_pk_fma_f32 v[4:5], v[86:87], v[60:61], v[4:5] op_sel_hi:[0,1,1]
	s_waitcnt vmcnt(2)
	v_pk_fma_f32 v[2:3], v[86:87], v[62:63], v[2:3] op_sel:[1,0,0]
	v_pk_fma_f32 v[4:5], v[86:87], v[64:65], v[4:5] op_sel:[1,0,0]
	s_waitcnt vmcnt(1)
	v_pk_fma_f32 v[2:3], v[88:89], v[66:67], v[2:3] op_sel_hi:[0,1,1]
	v_pk_fma_f32 v[4:5], v[88:89], v[68:69], v[4:5] op_sel_hi:[0,1,1]
	s_waitcnt vmcnt(0)
	v_pk_fma_f32 v[2:3], v[88:89], v[70:71], v[2:3] op_sel:[1,0,0]
	v_pk_fma_f32 v[4:5], v[88:89], v[72:73], v[4:5] op_sel:[1,0,0]
	s_cbranch_scc0 .LBB7_93
	v_mul_u32_u24_e32 v6, 12, v8
	v_lshlrev_b32_e32 v6, 2, v6
	global_load_dwordx4 v[10:13], v6, s[14:15]
	global_load_dwordx4 v[14:17], v6, s[14:15] offset:16
	global_load_dwordx4 v[18:21], v6, s[14:15] offset:32
	v_max_f32_e32 v3, v3, v3
	v_max_f32_e32 v2, v2, v2
	v_max_f32_e32 v6, v4, v4
	v_max_f32_e32 v4, 0, v3
	v_max_f32_e32 v2, 0, v2
	v_max_f32_e32 v5, v5, v5
	v_max_f32_e32 v6, 0, v6
	v_max_f32_e32 v22, 0, v5
	v_cmp_eq_u32_e32 vcc, 0, v8
	s_waitcnt vmcnt(2)
	v_mov_b32_e32 v24, v13
	s_waitcnt vmcnt(1)
	v_mul_f32_e32 v7, v4, v15
	v_mov_b32_e32 v25, v14
	v_fmac_f32_e32 v7, v2, v12
	v_pk_mul_f32 v[4:5], v[4:5], v[24:25] op_sel_hi:[0,1]
	s_waitcnt vmcnt(0)
	v_fmac_f32_e32 v7, v6, v18
	v_pk_fma_f32 v[2:3], v[2:3], v[10:11], v[4:5] op_sel_hi:[0,1,1]
	v_fmac_f32_e32 v7, v22, v21
	v_mov_b32_e32 v26, v19
	v_mov_b32_e32 v27, v20
	v_pk_fma_f32 v[2:3], v[6:7], v[16:17], v[2:3] op_sel_hi:[0,1,1]
	v_pk_fma_f32 v[2:3], v[22:23], v[26:27], v[2:3] op_sel_hi:[0,1,1]
	v_mov_b32_e32 v6, v7
	v_mov_b32_e32 v4, v2
	v_mov_b32_e32 v5, v3
	v_mov_b32_dpp v6, v6 quad_perm:[1,0,3,2] row_mask:0xf bank_mask:0xf
	v_mov_b32_dpp v4, v4 quad_perm:[1,0,3,2] row_mask:0xf bank_mask:0xf
	v_mov_b32_dpp v5, v5 quad_perm:[1,0,3,2] row_mask:0xf bank_mask:0xf
	v_add_f32_e32 v6, v7, v6
	v_pk_add_f32 v[2:3], v[2:3], v[4:5]
	v_mov_b32_e32 v7, v6
	v_mov_b32_e32 v4, v2
	v_mov_b32_e32 v5, v3
	v_mov_b32_dpp v7, v7 quad_perm:[2,3,0,1] row_mask:0xf bank_mask:0xf
	v_mov_b32_dpp v4, v4 quad_perm:[2,3,0,1] row_mask:0xf bank_mask:0xf
	v_mov_b32_dpp v5, v5 quad_perm:[2,3,0,1] row_mask:0xf bank_mask:0xf
	v_add_f32_e32 v6, v6, v7
	v_pk_add_f32 v[2:3], v[2:3], v[4:5]
	v_mov_b32_e32 v7, v6
	v_mov_b32_e32 v4, v2
	v_mov_b32_e32 v5, v3
	v_mov_b32_dpp v7, v7 row_half_mirror row_mask:0xf bank_mask:0xf
	v_mov_b32_dpp v4, v4 row_half_mirror row_mask:0xf bank_mask:0xf
	v_mov_b32_dpp v5, v5 row_half_mirror row_mask:0xf bank_mask:0xf
	s_and_saveexec_b64 s[4:5], vcc
	s_xor_b64 s[4:5], exec, s[4:5]
	s_cbranch_execz .LBB7_96
	v_or_b32_e32 v1, s3, v1
	s_load_dwordx2 s[4:5], s[16:17], 0x0
	s_load_dword s3, s[16:17], 0x8
	v_add_f32_e32 v8, v6, v7
	v_pk_add_f32 v[2:3], v[2:3], v[4:5]
	v_mad_u64_u32 v[6:7], s[6:7], v1, 12, s[18:19]
	s_waitcnt lgkmcnt(0)
	v_pk_add_f32 v[2:3], v[2:3], s[4:5]
	v_add_f32_e32 v4, s3, v8
	global_store_dwordx3 v[6:7], v[2:4], off

	.amdhsa_kernel _Z7k_layerILi2EEvPKiS1_PKfS3_PKDF16_S3_S5_S5_PDF16_P15HIP_vector_typeIfLj4EES9_S3_S3_S3_S3_S3_S3_PfSA_
		.amdhsa_group_segment_fixed_size 19456
		.amdhsa_private_segment_fixed_size 0
		.amdhsa_kernarg_size 152
		.amdhsa_user_sgpr_count 2
		.amdhsa_user_sgpr_dispatch_ptr 0
		.amdhsa_user_sgpr_queue_ptr 0
		.amdhsa_user_sgpr_kernarg_segment_ptr 1
		.amdhsa_user_sgpr_dispatch_id 0
		.amdhsa_user_sgpr_kernarg_preload_length 0
		.amdhsa_user_sgpr_kernarg_preload_offset 0
		.amdhsa_user_sgpr_private_segment_size 0
		.amdhsa_uses_dynamic_stack 0
		.amdhsa_enable_private_segment 0
		.amdhsa_system_sgpr_workgroup_id_x 1
		.amdhsa_system_sgpr_workgroup_id_y 0
		.amdhsa_system_sgpr_workgroup_id_z 0
		.amdhsa_system_sgpr_workgroup_info 0
		.amdhsa_system_vgpr_workitem_id 0
		.amdhsa_next_free_vgpr 96
		.amdhsa_next_free_sgpr 68
		.amdhsa_accum_offset 96
		.amdhsa_reserve_vcc 1
		.amdhsa_float_round_mode_32 0
		.amdhsa_float_round_mode_16_64 0
		.amdhsa_float_denorm_mode_32 3
		.amdhsa_float_denorm_mode_16_64 3
		.amdhsa_dx10_clamp 1
		.amdhsa_ieee_mode 1
		.amdhsa_fp16_overflow 0
		.amdhsa_tg_split 0
		.amdhsa_exception_fp_ieee_invalid_op 0
		.amdhsa_exception_fp_denorm_src 0
		.amdhsa_exception_fp_ieee_div_zero 0
		.amdhsa_exception_fp_ieee_overflow 0
		.amdhsa_exception_fp_ieee_underflow 0
		.amdhsa_exception_fp_ieee_inexact 0
		.amdhsa_exception_int_div_zero 0
	.end_amdhsa_kernel

amdhsa.kernels:
  - .agpr_count:     0
    .args:
      - .actual_access:  read_only
        .address_space:  global
        .offset:         0
        .size:           8
        .value_kind:     global_buffer
      - .actual_access:  write_only
        .address_space:  global
        .offset:         8
        .size:           8
        .value_kind:     global_buffer
      - .actual_access:  read_only
        .address_space:  global
        .offset:         16
        .size:           8
        .value_kind:     global_buffer
      - .actual_access:  read_only
        .address_space:  global
        .offset:         24
        .size:           8
        .value_kind:     global_buffer
      - .actual_access:  read_only
        .address_space:  global
        .offset:         32
        .size:           8
        .value_kind:     global_buffer
      - .actual_access:  read_only
        .address_space:  global
        .offset:         40
        .size:           8
        .value_kind:     global_buffer
      - .actual_access:  read_only
        .address_space:  global
        .offset:         48
        .size:           8
        .value_kind:     global_buffer
      - .actual_access:  read_only
        .address_space:  global
        .offset:         56
        .size:           8
        .value_kind:     global_buffer
      - .actual_access:  read_only
        .address_space:  global
        .offset:         64
        .size:           8
        .value_kind:     global_buffer
      - .actual_access:  read_only
        .address_space:  global
        .offset:         72
        .size:           8
        .value_kind:     global_buffer
      - .actual_access:  read_only
        .address_space:  global
        .offset:         80
        .size:           8
        .value_kind:     global_buffer
      - .actual_access:  write_only
        .address_space:  global
        .offset:         88
        .size:           8
        .value_kind:     global_buffer
      - .actual_access:  write_only
        .address_space:  global
        .offset:         96
        .size:           8
        .value_kind:     global_buffer
      - .actual_access:  write_only
        .address_space:  global
        .offset:         104
        .size:           8
        .value_kind:     global_buffer
      - .actual_access:  write_only
        .address_space:  global
        .offset:         112
        .size:           8
        .value_kind:     global_buffer
      - .actual_access:  write_only
        .address_space:  global
        .offset:         120
        .size:           8
        .value_kind:     global_buffer
    .group_segment_fixed_size: 1564
    .kernarg_segment_align: 8
    .kernarg_segment_size: 128
    .language:       OpenCL C
    .language_version:
      - 2
      - 0
    .max_flat_workgroup_size: 1024
    .name:           _Z6k_pre1PKiPiPKfS3_S3_S3_S3_S3_S3_S3_S3_PDF16_S4_S4_PfS5_
    .private_segment_fixed_size: 0
    .sgpr_count:     26
    .sgpr_spill_count: 0
    .symbol:         _Z6k_pre1PKiPiPKfS3_S3_S3_S3_S3_S3_S3_S3_PDF16_S4_S4_PfS5_.kd
    .uniform_work_group_size: 1
    .uses_dynamic_stack: false
    .vgpr_count:     64
    .vgpr_spill_count: 0
    .wavefront_size: 64
  - .agpr_count:     0
    .args:
      - .actual_access:  read_only
        .address_space:  global
        .offset:         0
        .size:           8
        .value_kind:     global_buffer
      - .actual_access:  read_only
        .address_space:  global
        .offset:         8
        .size:           8
        .value_kind:     global_buffer
      - .actual_access:  read_only
        .address_space:  global
        .offset:         16
        .size:           8
        .value_kind:     global_buffer
      - .actual_access:  read_only
        .address_space:  global
        .offset:         24
        .size:           8
        .value_kind:     global_buffer
      - .actual_access:  write_only
        .address_space:  global
        .offset:         32
        .size:           8
        .value_kind:     global_buffer
      - .actual_access:  write_only
        .address_space:  global
        .offset:         40
        .size:           8
        .value_kind:     global_buffer
    .group_segment_fixed_size: 1632
    .kernarg_segment_align: 8
    .kernarg_segment_size: 48
    .language:       OpenCL C
    .language_version:
      - 2
      - 0
    .max_flat_workgroup_size: 1024
    .name:           _Z9k_scatterPKiS0_S0_S0_PiS1_
    .private_segment_fixed_size: 0
    .sgpr_count:     22
    .sgpr_spill_count: 0
    .symbol:         _Z9k_scatterPKiS0_S0_S0_PiS1_.kd
    .uniform_work_group_size: 1
    .uses_dynamic_stack: false
    .vgpr_count:     50
    .vgpr_spill_count: 0
    .wavefront_size: 64
  - .agpr_count:     0
    .args:
      - .actual_access:  read_only
        .address_space:  global
        .offset:         0
        .size:           8
        .value_kind:     global_buffer
      - .actual_access:  read_only
        .address_space:  global
        .offset:         8
        .size:           8
        .value_kind:     global_buffer
      - .actual_access:  write_only
        .address_space:  global
        .offset:         16
        .size:           8
        .value_kind:     global_buffer
      - .actual_access:  write_only
        .address_space:  global
        .offset:         24
        .size:           8
        .value_kind:     global_buffer
      - .actual_access:  read_only
        .address_space:  global
        .offset:         32
        .size:           8
        .value_kind:     global_buffer
      - .actual_access:  read_only
        .address_space:  global
        .offset:         40
        .size:           8
        .value_kind:     global_buffer
      - .actual_access:  read_only
        .address_space:  global
        .offset:         48
        .size:           8
        .value_kind:     global_buffer
      - .actual_access:  read_only
        .address_space:  global
        .offset:         56
        .size:           8
        .value_kind:     global_buffer
      - .actual_access:  write_only
        .address_space:  global
        .offset:         64
        .size:           8
        .value_kind:     global_buffer
      - .actual_access:  write_only
        .address_space:  global
        .offset:         72
        .size:           8
        .value_kind:     global_buffer
      - .actual_access:  write_only
        .address_space:  global
        .offset:         80
        .size:           8
        .value_kind:     global_buffer
    .group_segment_fixed_size: 38720
    .kernarg_segment_align: 8
    .kernarg_segment_size: 88
    .language:       OpenCL C
    .language_version:
      - 2
      - 0
    .max_flat_workgroup_size: 1024
    .name:           _Z5k_csrPKiS0_PiS1_PKfS3_S3_S3_PDF16_P15HIP_vector_typeIfLj4EES7_
    .private_segment_fixed_size: 0
    .sgpr_count:     86
    .sgpr_spill_count: 0
    .symbol:         _Z5k_csrPKiS0_PiS1_PKfS3_S3_S3_PDF16_P15HIP_vector_typeIfLj4EES7_.kd
    .uniform_work_group_size: 1
    .uses_dynamic_stack: false
    .vgpr_count:     64
    .vgpr_spill_count: 0
    .wavefront_size: 64
  - .agpr_count:     0
    .args:
      - .actual_access:  read_only
        .address_space:  global
        .offset:         0
        .size:           8
        .value_kind:     global_buffer
      - .actual_access:  write_only
        .address_space:  global
        .offset:         8
        .size:           8
        .value_kind:     global_buffer
      - .actual_access:  write_only
        .address_space:  global
        .offset:         16
        .size:           8
        .value_kind:     global_buffer
    .group_segment_fixed_size: 16
    .kernarg_segment_align: 8
    .kernarg_segment_size: 24
    .language:       OpenCL C
    .language_version:
      - 2
      - 0
    .max_flat_workgroup_size: 256
    .name:           _Z6k_pre2PKiPiS1_
    .private_segment_fixed_size: 0
    .sgpr_count:     14
    .sgpr_spill_count: 0
    .symbol:         _Z6k_pre2PKiPiS1_.kd
    .uniform_work_group_size: 1
    .uses_dynamic_stack: false
    .vgpr_count:     14
    .vgpr_spill_count: 0
    .wavefront_size: 64
  - .agpr_count:     0
    .args:
      - .actual_access:  read_only
        .address_space:  global
        .offset:         0
        .size:           8
        .value_kind:     global_buffer
      - .actual_access:  read_only
        .address_space:  global
        .offset:         8
        .size:           8
        .value_kind:     global_buffer
      - .actual_access:  read_only
        .address_space:  global
        .offset:         16
        .size:           8
        .value_kind:     global_buffer
      - .actual_access:  read_only
        .address_space:  global
        .offset:         24
        .size:           8
        .value_kind:     global_buffer
      - .actual_access:  read_only
        .address_space:  global
        .offset:         32
        .size:           8
        .value_kind:     global_buffer
      - .actual_access:  write_only
        .address_space:  global
        .offset:         40
        .size:           8
        .value_kind:     global_buffer
    .group_segment_fixed_size: 1408
    .kernarg_segment_align: 8
    .kernarg_segment_size: 48
    .language:       OpenCL C
    .language_version:
      - 2
      - 0
    .max_flat_workgroup_size: 256
    .name:           _Z7k_finalPKfS0_S0_S0_S0_Pf
    .private_segment_fixed_size: 0
    .sgpr_count:     26
    .sgpr_spill_count: 0
    .symbol:         _Z7k_finalPKfS0_S0_S0_S0_Pf.kd
    .uniform_work_group_size: 1
    .uses_dynamic_stack: false
    .vgpr_count:     96
    .vgpr_spill_count: 0
    .wavefront_size: 64
  - .agpr_count:     0
    .args:
      - .actual_access:  read_only
        .address_space:  global
        .offset:         0
        .size:           8
        .value_kind:     global_buffer
      - .actual_access:  read_only
        .address_space:  global
        .offset:         8
        .size:           8
        .value_kind:     global_buffer
      - .actual_access:  read_only
        .address_space:  global
        .offset:         16
        .size:           8
        .value_kind:     global_buffer
      - .actual_access:  read_only
        .address_space:  global
        .offset:         24
        .size:           8
        .value_kind:     global_buffer
      - .actual_access:  read_only
        .address_space:  global
        .offset:         32
        .size:           8
        .value_kind:     global_buffer
      - .actual_access:  read_only
        .address_space:  global
        .offset:         40
        .size:           8
        .value_kind:     global_buffer
      - .actual_access:  read_only
        .address_space:  global
        .offset:         48
        .size:           8
        .value_kind:     global_buffer
      - .actual_access:  read_only
        .address_space:  global
        .offset:         56
        .size:           8
        .value_kind:     global_buffer
      - .actual_access:  write_only
        .address_space:  global
        .offset:         64
        .size:           8
        .value_kind:     global_buffer
      - .actual_access:  write_only
        .address_space:  global
        .offset:         72
        .size:           8
        .value_kind:     global_buffer
      - .actual_access:  write_only
        .address_space:  global
        .offset:         80
        .size:           8
        .value_kind:     global_buffer
      - .actual_access:  read_only
        .address_space:  global
        .offset:         88
        .size:           8
        .value_kind:     global_buffer
      - .actual_access:  read_only
        .address_space:  global
        .offset:         96
        .size:           8
        .value_kind:     global_buffer
      - .actual_access:  read_only
        .address_space:  global
        .offset:         104
        .size:           8
        .value_kind:     global_buffer
      - .actual_access:  read_only
        .address_space:  global
        .offset:         112
        .size:           8
        .value_kind:     global_buffer
      - .actual_access:  read_only
        .address_space:  global
        .offset:         120
        .size:           8
        .value_kind:     global_buffer
      - .actual_access:  read_only
        .address_space:  global
        .offset:         128
        .size:           8
        .value_kind:     global_buffer
      - .actual_access:  read_only
        .address_space:  global
        .offset:         136
        .size:           8
        .value_kind:     global_buffer
      - .actual_access:  read_only
        .address_space:  global
        .offset:         144
        .size:           8
        .value_kind:     global_buffer
    .group_segment_fixed_size: 29248
    .kernarg_segment_align: 8
    .kernarg_segment_size: 152
    .language:       OpenCL C
    .language_version:
      - 2
      - 0
    .max_flat_workgroup_size: 256
    .name:           _Z7k_layerILi0EEvPKiS1_PKfS3_PKDF16_S3_S5_S5_PDF16_P15HIP_vector_typeIfLj4EES9_S3_S3_S3_S3_S3_S3_PfSA_
    .private_segment_fixed_size: 0
    .sgpr_count:     66
    .sgpr_spill_count: 0
    .symbol:         _Z7k_layerILi0EEvPKiS1_PKfS3_PKDF16_S3_S5_S5_PDF16_P15HIP_vector_typeIfLj4EES9_S3_S3_S3_S3_S3_S3_PfSA_.kd
    .uniform_work_group_size: 1
    .uses_dynamic_stack: false
    .vgpr_count:     86
    .vgpr_spill_count: 0
    .wavefront_size: 64
  - .agpr_count:     0
    .args:
      - .actual_access:  read_only
        .address_space:  global
        .offset:         0
        .size:           8
        .value_kind:     global_buffer
      - .actual_access:  read_only
        .address_space:  global
        .offset:         8
        .size:           8
        .value_kind:     global_buffer
      - .actual_access:  read_only
        .address_space:  global
        .offset:         16
        .size:           8
        .value_kind:     global_buffer
      - .actual_access:  read_only
        .address_space:  global
        .offset:         24
        .size:           8
        .value_kind:     global_buffer
      - .actual_access:  read_only
        .address_space:  global
        .offset:         32
        .size:           8
        .value_kind:     global_buffer
      - .actual_access:  read_only
        .address_space:  global
        .offset:         40
        .size:           8
        .value_kind:     global_buffer
      - .actual_access:  read_only
        .address_space:  global
        .offset:         48
        .size:           8
        .value_kind:     global_buffer
      - .actual_access:  read_only
        .address_space:  global
        .offset:         56
        .size:           8
        .value_kind:     global_buffer
      - .actual_access:  write_only
        .address_space:  global
        .offset:         64
        .size:           8
        .value_kind:     global_buffer
      - .actual_access:  write_only
        .address_space:  global
        .offset:         72
        .size:           8
        .value_kind:     global_buffer
      - .actual_access:  write_only
        .address_space:  global
        .offset:         80
        .size:           8
        .value_kind:     global_buffer
      - .actual_access:  read_only
        .address_space:  global
        .offset:         88
        .size:           8
        .value_kind:     global_buffer
      - .actual_access:  read_only
        .address_space:  global
        .offset:         96
        .size:           8
        .value_kind:     global_buffer
      - .actual_access:  read_only
        .address_space:  global
        .offset:         104
        .size:           8
        .value_kind:     global_buffer
      - .actual_access:  read_only
        .address_space:  global
        .offset:         112
        .size:           8
        .value_kind:     global_buffer
      - .actual_access:  read_only
        .address_space:  global
        .offset:         120
        .size:           8
        .value_kind:     global_buffer
      - .actual_access:  read_only
        .address_space:  global
        .offset:         128
        .size:           8
        .value_kind:     global_buffer
      - .actual_access:  read_only
        .address_space:  global
        .offset:         136
        .size:           8
        .value_kind:     global_buffer
      - .actual_access:  read_only
        .address_space:  global
        .offset:         144
        .size:           8
        .value_kind:     global_buffer
    .group_segment_fixed_size: 21504
    .kernarg_segment_align: 8
    .kernarg_segment_size: 152
    .language:       OpenCL C
    .language_version:
      - 2
      - 0
    .max_flat_workgroup_size: 256
    .name:           _Z7k_layerILi1EEvPKiS1_PKfS3_PKDF16_S3_S5_S5_PDF16_P15HIP_vector_typeIfLj4EES9_S3_S3_S3_S3_S3_S3_PfSA_
    .private_segment_fixed_size: 0
    .sgpr_count:     70
    .sgpr_spill_count: 0
    .symbol:         _Z7k_layerILi1EEvPKiS1_PKfS3_PKDF16_S3_S5_S5_PDF16_P15HIP_vector_typeIfLj4EES9_S3_S3_S3_S3_S3_S3_PfSA_.kd
    .uniform_work_group_size: 1
    .uses_dynamic_stack: false
    .vgpr_count:     96
    .vgpr_spill_count: 0
    .wavefront_size: 64
  - .agpr_count:     0
    .args:
      - .actual_access:  read_only
        .address_space:  global
        .offset:         0
        .size:           8
        .value_kind:     global_buffer
      - .actual_access:  read_only
        .address_space:  global
        .offset:         8
        .size:           8
        .value_kind:     global_buffer
      - .actual_access:  read_only
        .address_space:  global
        .offset:         16
        .size:           8
        .value_kind:     global_buffer
      - .actual_access:  read_only
        .address_space:  global
        .offset:         24
        .size:           8
        .value_kind:     global_buffer
      - .actual_access:  read_only
        .address_space:  global
        .offset:         32
        .size:           8
        .value_kind:     global_buffer
      - .actual_access:  read_only
        .address_space:  global
        .offset:         40
        .size:           8
        .value_kind:     global_buffer
      - .actual_access:  read_only
        .address_space:  global
        .offset:         48
        .size:           8
        .value_kind:     global_buffer
      - .actual_access:  read_only
        .address_space:  global
        .offset:         56
        .size:           8
        .value_kind:     global_buffer
      - .actual_access:  read_only
        .address_space:  global
        .offset:         64
        .size:           8
        .value_kind:     global_buffer
      - .actual_access:  read_only
        .address_space:  global
        .offset:         72
        .size:           8
        .value_kind:     global_buffer
      - .actual_access:  read_only
        .address_space:  global
        .offset:         80
        .size:           8
        .value_kind:     global_buffer
      - .actual_access:  read_only
        .address_space:  global
        .offset:         88
        .size:           8
        .value_kind:     global_buffer
      - .actual_access:  read_only
        .address_space:  global
        .offset:         96
        .size:           8
        .value_kind:     global_buffer
      - .actual_access:  read_only
        .address_space:  global
        .offset:         104
        .size:           8
        .value_kind:     global_buffer
      - .actual_access:  read_only
        .address_space:  global
        .offset:         112
        .size:           8
        .value_kind:     global_buffer
      - .actual_access:  read_only
        .address_space:  global
        .offset:         120
        .size:           8
        .value_kind:     global_buffer
      - .actual_access:  read_only
        .address_space:  global
        .offset:         128
        .size:           8
        .value_kind:     global_buffer
      - .actual_access:  write_only
        .address_space:  global
        .offset:         136
        .size:           8
        .value_kind:     global_buffer
      - .address_space:  global
        .offset:         144
        .size:           8
        .value_kind:     global_buffer
    .group_segment_fixed_size: 19456
    .kernarg_segment_align: 8
    .kernarg_segment_size: 152
    .language:       OpenCL C
    .language_version:
      - 2
      - 0
    .max_flat_workgroup_size: 256
    .name:           _Z7k_layerILi2EEvPKiS1_PKfS3_PKDF16_S3_S5_S5_PDF16_P15HIP_vector_typeIfLj4EES9_S3_S3_S3_S3_S3_S3_PfSA_
    .private_segment_fixed_size: 0
    .sgpr_count:     74
    .sgpr_spill_count: 0
    .symbol:         _Z7k_layerILi2EEvPKiS1_PKfS3_PKDF16_S3_S5_S5_PDF16_P15HIP_vector_typeIfLj4EES9_S3_S3_S3_S3_S3_S3_PfSA_.kd
    .uniform_work_group_size: 1
    .uses_dynamic_stack: false
    .vgpr_count:     96
    .vgpr_spill_count: 0
    .wavefront_size: 64
